# PEER select: rank of the 50 candidate sums via LDS key list + broadcast ds_read_b128 (2 VALU per candidate), on top of the survivor-rank rewrite
# speedup vs baseline: 1.0258x; 1.0045x over previous
; __device__ __forceinline__ void rank5(int& rc, unsigned e0, unsigned e1, unsigned e2, unsigned e3, unsigned e4, unsigned ck) {
;     asm volatile("s_nop 1\n\t"
;                  "v_cmp_gt_u32_e64 s[80:81], %1, %6\n\t" "v_cmp_gt_u32_e64 s[82:83], %2, %6\n\t" "v_cmp_gt_u32_e64 s[84:85], %3, %6\n\t" "v_cmp_gt_u32_e64 s[86:87], %4, %6\n\t" "v_cmp_gt_u32_e64 s[88:89], %5, %6\n\t"
;                  "v_addc_co_u32_e64 %0, s[96:97], 0, %0, s[80:81]\n\t" "v_addc_co_u32_e64 %0, s[96:97], 0, %0, s[82:83]\n\t" "v_addc_co_u32_e64 %0, s[96:97], 0, %0, s[84:85]\n\t"
;                  "v_addc_co_u32_e64 %0, s[96:97], 0, %0, s[86:87]\n\t" "v_addc_co_u32_e64 %0, s[96:97], 0, %0, s[88:89]"
;                  : "+v"(rc) : "s"(e0), "s"(e1), "s"(e2), "s"(e3), "s"(e4), "v"(ck)
;                  : "s80", "s81", "s82", "s83", "s84", "s85", "s86", "s87", "s88", "s89", "s96", "s97");
; }
; __device__ __forceinline__ void peer_select_phase(const Args& a, int layer, LAS unsigned char* lds, int G, int bid) {
;     ...
; #pragma unroll 2
;         for (int m = 0; m < 50; m += 5) rank5(rc, (unsigned)__builtin_amdgcn_readlane((int)ck, m), (unsigned)__builtin_amdgcn_readlane((int)ck, m + 1), (unsigned)__builtin_amdgcn_readlane((int)ck, m + 2),
;                                               (unsigned)__builtin_amdgcn_readlane((int)ck, m + 3), (unsigned)__builtin_amdgcn_readlane((int)ck, m + 4), ck);
;         if (lane < 50 && rc < 16) { SV[32 + rc] = cv; SI[32 + rc] = ci * 16 + cj; }
.LBB0_1115:
	s_lshl_b32 s100, s46, 1
	s_add_i32 s100, s100, 0xfffe1800
	v_mbcnt_lo_u32_b32 v164, -1, 0
	v_mbcnt_hi_u32_b32 v164, -1, v164
	v_lshl_add_u32 v164, v164, 2, s100
	ds_write_b32 v164, v138
	v_mov_b32_e32 v164, s100
	v_mov_b32_e32 v165, 0
	s_waitcnt lgkmcnt(0)
	ds_read_b128 v[168:171], v164
	ds_read_b128 v[172:175], v164 offset:16
	ds_read_b128 v[176:179], v164 offset:32
	ds_read_b128 v[180:183], v164 offset:48
	ds_read_b128 v[184:187], v164 offset:64
	ds_read_b128 v[188:191], v164 offset:80
	ds_read_b128 v[192:195], v164 offset:96
	ds_read_b128 v[196:199], v164 offset:112
	ds_read_b128 v[200:203], v164 offset:128
	ds_read_b128 v[204:207], v164 offset:144
	ds_read_b128 v[208:211], v164 offset:160
	ds_read_b128 v[212:215], v164 offset:176
	ds_read_b128 v[216:219], v164 offset:192
	s_waitcnt lgkmcnt(11)
	v_cmp_gt_u32_e64 s[80:81], v168, v138
	v_cmp_gt_u32_e64 s[82:83], v169, v138
	v_cmp_gt_u32_e64 s[84:85], v170, v138
	v_cmp_gt_u32_e64 s[86:87], v171, v138
	v_addc_co_u32_e64 v136, s[96:97], 0, v136, s[80:81]
	v_addc_co_u32_e64 v136, s[96:97], 0, v136, s[82:83]
	v_addc_co_u32_e64 v136, s[96:97], 0, v136, s[84:85]
	v_addc_co_u32_e64 v136, s[96:97], 0, v136, s[86:87]
	v_cmp_gt_u32_e64 s[80:81], v172, v138
	v_cmp_gt_u32_e64 s[82:83], v173, v138
	v_cmp_gt_u32_e64 s[84:85], v174, v138
	v_cmp_gt_u32_e64 s[86:87], v175, v138
	v_addc_co_u32_e64 v165, s[96:97], 0, v165, s[80:81]
	v_addc_co_u32_e64 v165, s[96:97], 0, v165, s[82:83]
	v_addc_co_u32_e64 v165, s[96:97], 0, v165, s[84:85]
	v_addc_co_u32_e64 v165, s[96:97], 0, v165, s[86:87]
	s_waitcnt lgkmcnt(9)
	v_cmp_gt_u32_e64 s[80:81], v176, v138
	v_cmp_gt_u32_e64 s[82:83], v177, v138
	v_cmp_gt_u32_e64 s[84:85], v178, v138
	v_cmp_gt_u32_e64 s[86:87], v179, v138
	v_addc_co_u32_e64 v136, s[96:97], 0, v136, s[80:81]
	v_addc_co_u32_e64 v136, s[96:97], 0, v136, s[82:83]
	v_addc_co_u32_e64 v136, s[96:97], 0, v136, s[84:85]
	v_addc_co_u32_e64 v136, s[96:97], 0, v136, s[86:87]
	v_cmp_gt_u32_e64 s[80:81], v180, v138
	v_cmp_gt_u32_e64 s[82:83], v181, v138
	v_cmp_gt_u32_e64 s[84:85], v182, v138
	v_cmp_gt_u32_e64 s[86:87], v183, v138
	v_addc_co_u32_e64 v165, s[96:97], 0, v165, s[80:81]
	v_addc_co_u32_e64 v165, s[96:97], 0, v165, s[82:83]
	v_addc_co_u32_e64 v165, s[96:97], 0, v165, s[84:85]
	v_addc_co_u32_e64 v165, s[96:97], 0, v165, s[86:87]
	s_waitcnt lgkmcnt(7)
	v_cmp_gt_u32_e64 s[80:81], v184, v138
	v_cmp_gt_u32_e64 s[82:83], v185, v138
	v_cmp_gt_u32_e64 s[84:85], v186, v138
	v_cmp_gt_u32_e64 s[86:87], v187, v138
	v_addc_co_u32_e64 v136, s[96:97], 0, v136, s[80:81]
	v_addc_co_u32_e64 v136, s[96:97], 0, v136, s[82:83]
	v_addc_co_u32_e64 v136, s[96:97], 0, v136, s[84:85]
	v_addc_co_u32_e64 v136, s[96:97], 0, v136, s[86:87]
	v_cmp_gt_u32_e64 s[80:81], v188, v138
	v_cmp_gt_u32_e64 s[82:83], v189, v138
	v_cmp_gt_u32_e64 s[84:85], v190, v138
	v_cmp_gt_u32_e64 s[86:87], v191, v138
	v_addc_co_u32_e64 v165, s[96:97], 0, v165, s[80:81]
	v_addc_co_u32_e64 v165, s[96:97], 0, v165, s[82:83]
	v_addc_co_u32_e64 v165, s[96:97], 0, v165, s[84:85]
	v_addc_co_u32_e64 v165, s[96:97], 0, v165, s[86:87]
	s_waitcnt lgkmcnt(5)
	v_cmp_gt_u32_e64 s[80:81], v192, v138
	v_cmp_gt_u32_e64 s[82:83], v193, v138
	v_cmp_gt_u32_e64 s[84:85], v194, v138
	v_cmp_gt_u32_e64 s[86:87], v195, v138
	v_addc_co_u32_e64 v136, s[96:97], 0, v136, s[80:81]
	v_addc_co_u32_e64 v136, s[96:97], 0, v136, s[82:83]
	v_addc_co_u32_e64 v136, s[96:97], 0, v136, s[84:85]
	v_addc_co_u32_e64 v136, s[96:97], 0, v136, s[86:87]
	v_cmp_gt_u32_e64 s[80:81], v196, v138
	v_cmp_gt_u32_e64 s[82:83], v197, v138
	v_cmp_gt_u32_e64 s[84:85], v198, v138
	v_cmp_gt_u32_e64 s[86:87], v199, v138
	v_addc_co_u32_e64 v165, s[96:97], 0, v165, s[80:81]
	v_addc_co_u32_e64 v165, s[96:97], 0, v165, s[82:83]
	v_addc_co_u32_e64 v165, s[96:97], 0, v165, s[84:85]
	v_addc_co_u32_e64 v165, s[96:97], 0, v165, s[86:87]
	s_waitcnt lgkmcnt(3)
; #define LDS_WAIT() asm volatile("s_waitcnt lgkmcnt(0)" ::: "memory")
; __device__ __forceinline__ void peer_select_phase(const Args& a, int layer, LAS unsigned char* lds, int G, int bid) {
;     ...
; #pragma unroll 2
;         for (int m = 0; m < 50; m += 5) rank5(rc, (unsigned)__builtin_amdgcn_readlane((int)ck, m), (unsigned)__builtin_amdgcn_readlane((int)ck, m + 1), (unsigned)__builtin_amdgcn_readlane((int)ck, m + 2),
;                                               (unsigned)__builtin_amdgcn_readlane((int)ck, m + 3), (unsigned)__builtin_amdgcn_readlane((int)ck, m + 4), ck);
;         if (lane < 50 && rc < 16) { SV[32 + rc] = cv; SI[32 + rc] = ci * 16 + cj; }
;         LDS_WAIT();
;         {
;             const int ll = lane & 15;
;             const float ts = SV[32 + ll]; const int tp = SI[32 + ll];
;             const int e1 = SI[(tp >> 4) & 15], e2 = SI[16 + (tp & 15)];
;             const float mx = SV[32];
;             const float ex = __expf(rstd_t * (ts - mx));
;             float sm = ex; sm += __shfl_xor(sm, 8); sm += __shfl_xor(sm, 4); sm += __shfl_xor(sm, 2); sm += __shfl_xor(sm, 1);
;             if (lane < 16) { IDX[(size_t)tok * 128 + hd * 16 + lane] = e1 * 128 + e2; GATE[(size_t)tok * 128 + hd * 16 + lane] = ex / sm; }
	v_cmp_gt_u32_e64 s[80:81], v200, v138
	v_cmp_gt_u32_e64 s[82:83], v201, v138
	v_cmp_gt_u32_e64 s[84:85], v202, v138
	v_cmp_gt_u32_e64 s[86:87], v203, v138
	v_addc_co_u32_e64 v136, s[96:97], 0, v136, s[80:81]
	v_addc_co_u32_e64 v136, s[96:97], 0, v136, s[82:83]
	v_addc_co_u32_e64 v136, s[96:97], 0, v136, s[84:85]
	v_addc_co_u32_e64 v136, s[96:97], 0, v136, s[86:87]
	v_cmp_gt_u32_e64 s[80:81], v204, v138
	v_cmp_gt_u32_e64 s[82:83], v205, v138
	v_cmp_gt_u32_e64 s[84:85], v206, v138
	v_cmp_gt_u32_e64 s[86:87], v207, v138
	v_addc_co_u32_e64 v165, s[96:97], 0, v165, s[80:81]
	v_addc_co_u32_e64 v165, s[96:97], 0, v165, s[82:83]
	v_addc_co_u32_e64 v165, s[96:97], 0, v165, s[84:85]
	v_addc_co_u32_e64 v165, s[96:97], 0, v165, s[86:87]
	s_waitcnt lgkmcnt(1)
	v_cmp_gt_u32_e64 s[80:81], v208, v138
	v_cmp_gt_u32_e64 s[82:83], v209, v138
	v_cmp_gt_u32_e64 s[84:85], v210, v138
	v_cmp_gt_u32_e64 s[86:87], v211, v138
	v_addc_co_u32_e64 v136, s[96:97], 0, v136, s[80:81]
	v_addc_co_u32_e64 v136, s[96:97], 0, v136, s[82:83]
	v_addc_co_u32_e64 v136, s[96:97], 0, v136, s[84:85]
	v_addc_co_u32_e64 v136, s[96:97], 0, v136, s[86:87]
	v_cmp_gt_u32_e64 s[80:81], v212, v138
	v_cmp_gt_u32_e64 s[82:83], v213, v138
	v_cmp_gt_u32_e64 s[84:85], v214, v138
	v_cmp_gt_u32_e64 s[86:87], v215, v138
	v_addc_co_u32_e64 v165, s[96:97], 0, v165, s[80:81]
	v_addc_co_u32_e64 v165, s[96:97], 0, v165, s[82:83]
	v_addc_co_u32_e64 v165, s[96:97], 0, v165, s[84:85]
	v_addc_co_u32_e64 v165, s[96:97], 0, v165, s[86:87]
	s_waitcnt lgkmcnt(0)
	v_cmp_gt_u32_e64 s[80:81], v216, v138
	v_cmp_gt_u32_e64 s[82:83], v217, v138
	v_cmp_gt_u32_e64 s[84:85], v218, v138
	v_cmp_gt_u32_e64 s[86:87], v219, v138
	v_addc_co_u32_e64 v136, s[96:97], 0, v136, s[80:81]
	v_addc_co_u32_e64 v136, s[96:97], 0, v136, s[82:83]
	v_addc_co_u32_e64 v136, s[96:97], 0, v136, s[84:85]
	v_addc_co_u32_e64 v136, s[96:97], 0, v136, s[86:87]
	v_add_u32_e32 v136, v136, v165
	v_cmp_gt_i32_e32 vcc, 16, v136
	s_and_b64 s[12:13], s[6:7], vcc
	s_and_saveexec_b64 s[10:11], s[12:13]
	v_lshl_add_u32 v136, v136, 2, s46
	ds_write2_b32 v136, v131, v150 offset0:32 offset1:80
	s_or_b64 exec, exec, s[10:11]
	s_waitcnt lgkmcnt(0)
	v_mov_b32_e32 v131, s46
	ds_read_b32 v136, v151 offset:128
	ds_read_b32 v131, v131 offset:128
	v_and_b32_e32 v139, 64, v135
	v_xor_b32_e32 v138, 8, v135
	v_xor_b32_e32 v142, 2, v135
	v_xor_b32_e32 v143, 1, v135
	s_waitcnt lgkmcnt(0)
	v_sub_f32_e32 v131, v136, v131
	v_mul_f32_e32 v131, v156, v131
	v_mul_f32_e32 v131, 0x3fb8aa3b, v131
	v_exp_f32_e32 v141, v131
	v_add_u32_e32 v136, 64, v139
	v_cmp_lt_i32_e32 vcc, v138, v136
	v_xor_b32_e32 v139, 4, v135
	s_nop 0
	v_cndmask_b32_e32 v131, v135, v138, vcc
	v_lshlrev_b32_e32 v131, 2, v131
	ds_bpermute_b32 v138, v131, v141
	v_cmp_lt_i32_e32 vcc, v139, v136
	s_waitcnt lgkmcnt(0)
	v_add_f32_e32 v140, v141, v138
	v_cndmask_b32_e32 v139, v135, v139, vcc
	v_lshlrev_b32_e32 v138, 2, v139
	ds_bpermute_b32 v139, v138, v140
	v_cmp_lt_i32_e32 vcc, v142, v136
	s_waitcnt lgkmcnt(0)
	v_add_f32_e32 v140, v140, v139
	v_cndmask_b32_e32 v142, v135, v142, vcc
	v_lshlrev_b32_e32 v139, 2, v142
	ds_bpermute_b32 v142, v139, v140
	v_cmp_lt_i32_e32 vcc, v143, v136
	s_waitcnt lgkmcnt(0)
	v_add_f32_e32 v142, v140, v142
	v_cndmask_b32_e32 v143, v135, v143, vcc
	v_lshlrev_b32_e32 v140, 2, v143
	ds_bpermute_b32 v143, v140, v142
	s_and_saveexec_b64 s[10:11], s[8:9]
	s_cbranch_execz .LBB0_1120
	ds_read_b32 v144, v151 offset:320
	s_waitcnt lgkmcnt(1)
	v_add_f32_e32 v156, v142, v143
	s_ashr_i32 s12, s58, 3
	v_div_scale_f32 v158, s[30:31], v156, v156, v141
	s_waitcnt lgkmcnt(0)
	v_and_b32_e32 v145, 15, v144
	v_lshrrev_b32_e32 v144, 2, v144
	v_and_b32_e32 v144, 60, v144
	v_lshl_add_u32 v145, v145, 2, s46
	v_add_u32_e32 v144, s46, v144
	ds_read_b32 v145, v145 offset:256
	ds_read_b32 v144, v144 offset:192
	s_ashr_i32 s13, s12, 31
	v_rcp_f32_e32 v159, v158
	s_lshl_b64 s[12:13], s[12:13], 9
	v_lshl_or_b32 v142, v134, 2, s12
	v_mov_b32_e32 v143, s13
	s_waitcnt lgkmcnt(0)
	v_lshl_add_u32 v157, v144, 7, v145
	v_lshl_add_u64 v[144:145], s[18:19], 0, v[142:143]
	global_store_dword v[144:145], v157, off
	v_fma_f32 v144, -v158, v159, 1.0
	v_fmac_f32_e32 v159, v144, v159
	v_div_scale_f32 v144, vcc, v141, v156, v141
	v_mul_f32_e32 v145, v144, v159
	v_fma_f32 v157, -v158, v145, v144
	v_fmac_f32_e32 v145, v157, v159
	v_fma_f32 v144, -v158, v145, v144
	v_div_fmas_f32 v144, v144, v159, v145
	v_div_fixup_f32 v141, v144, v156, v141
	v_lshl_add_u64 v[142:143], s[20:21], 0, v[142:143]
	global_store_dword v[142:143], v141, off

; __device__ __forceinline__ void rank5(int& rc, unsigned e0, unsigned e1, unsigned e2, unsigned e3, unsigned e4, unsigned ck) {
;     asm volatile("s_nop 1\n\t"
;                  "v_cmp_gt_u32_e64 s[80:81], %1, %6\n\t" "v_cmp_gt_u32_e64 s[82:83], %2, %6\n\t" "v_cmp_gt_u32_e64 s[84:85], %3, %6\n\t" "v_cmp_gt_u32_e64 s[86:87], %4, %6\n\t" "v_cmp_gt_u32_e64 s[88:89], %5, %6\n\t"
;                  "v_addc_co_u32_e64 %0, s[96:97], 0, %0, s[80:81]\n\t" "v_addc_co_u32_e64 %0, s[96:97], 0, %0, s[82:83]\n\t" "v_addc_co_u32_e64 %0, s[96:97], 0, %0, s[84:85]\n\t"
;                  "v_addc_co_u32_e64 %0, s[96:97], 0, %0, s[86:87]\n\t" "v_addc_co_u32_e64 %0, s[96:97], 0, %0, s[88:89]"
;                  : "+v"(rc) : "s"(e0), "s"(e1), "s"(e2), "s"(e3), "s"(e4), "v"(ck)
;                  : "s80", "s81", "s82", "s83", "s84", "s85", "s86", "s87", "s88", "s89", "s96", "s97");
; }
; __device__ __forceinline__ void peer_select_phase(const Args& a, int layer, LAS unsigned char* lds, int G, int bid) {
;     ...
; #pragma unroll 2
;         for (int m = 0; m < 50; m += 5) rank5(rc, (unsigned)__builtin_amdgcn_readlane((int)ck, m), (unsigned)__builtin_amdgcn_readlane((int)ck, m + 1), (unsigned)__builtin_amdgcn_readlane((int)ck, m + 2),
;                                               (unsigned)__builtin_amdgcn_readlane((int)ck, m + 3), (unsigned)__builtin_amdgcn_readlane((int)ck, m + 4), ck);
;         if (lane < 50 && rc < 16) { SV[32 + rc] = cv; SI[32 + rc] = ci * 16 + cj; }
.LBB0_2176:
	s_lshl_b32 s100, s50, 1
	s_add_i32 s100, s100, 0xfffe1800
	v_mbcnt_lo_u32_b32 v164, -1, 0
	v_mbcnt_hi_u32_b32 v164, -1, v164
	v_lshl_add_u32 v164, v164, 2, s100
	ds_write_b32 v164, v138
	v_mov_b32_e32 v164, s100
	v_mov_b32_e32 v165, 0
	s_waitcnt lgkmcnt(0)
	ds_read_b128 v[168:171], v164
	ds_read_b128 v[172:175], v164 offset:16
	ds_read_b128 v[176:179], v164 offset:32
	ds_read_b128 v[180:183], v164 offset:48
	ds_read_b128 v[184:187], v164 offset:64
	ds_read_b128 v[188:191], v164 offset:80
	ds_read_b128 v[192:195], v164 offset:96
	ds_read_b128 v[196:199], v164 offset:112
	ds_read_b128 v[200:203], v164 offset:128
	ds_read_b128 v[204:207], v164 offset:144
	ds_read_b128 v[208:211], v164 offset:160
	ds_read_b128 v[212:215], v164 offset:176
	ds_read_b128 v[216:219], v164 offset:192
	s_waitcnt lgkmcnt(11)
	v_cmp_gt_u32_e64 s[80:81], v168, v138
	v_cmp_gt_u32_e64 s[82:83], v169, v138
	v_cmp_gt_u32_e64 s[84:85], v170, v138
	v_cmp_gt_u32_e64 s[86:87], v171, v138
	v_addc_co_u32_e64 v136, s[96:97], 0, v136, s[80:81]
	v_addc_co_u32_e64 v136, s[96:97], 0, v136, s[82:83]
	v_addc_co_u32_e64 v136, s[96:97], 0, v136, s[84:85]
	v_addc_co_u32_e64 v136, s[96:97], 0, v136, s[86:87]
	v_cmp_gt_u32_e64 s[80:81], v172, v138
	v_cmp_gt_u32_e64 s[82:83], v173, v138
	v_cmp_gt_u32_e64 s[84:85], v174, v138
	v_cmp_gt_u32_e64 s[86:87], v175, v138
	v_addc_co_u32_e64 v165, s[96:97], 0, v165, s[80:81]
	v_addc_co_u32_e64 v165, s[96:97], 0, v165, s[82:83]
	v_addc_co_u32_e64 v165, s[96:97], 0, v165, s[84:85]
	v_addc_co_u32_e64 v165, s[96:97], 0, v165, s[86:87]
	s_waitcnt lgkmcnt(9)
	v_cmp_gt_u32_e64 s[80:81], v176, v138
	v_cmp_gt_u32_e64 s[82:83], v177, v138
	v_cmp_gt_u32_e64 s[84:85], v178, v138
	v_cmp_gt_u32_e64 s[86:87], v179, v138
	v_addc_co_u32_e64 v136, s[96:97], 0, v136, s[80:81]
	v_addc_co_u32_e64 v136, s[96:97], 0, v136, s[82:83]
	v_addc_co_u32_e64 v136, s[96:97], 0, v136, s[84:85]
	v_addc_co_u32_e64 v136, s[96:97], 0, v136, s[86:87]
	v_cmp_gt_u32_e64 s[80:81], v180, v138
	v_cmp_gt_u32_e64 s[82:83], v181, v138
	v_cmp_gt_u32_e64 s[84:85], v182, v138
	v_cmp_gt_u32_e64 s[86:87], v183, v138
	v_addc_co_u32_e64 v165, s[96:97], 0, v165, s[80:81]
	v_addc_co_u32_e64 v165, s[96:97], 0, v165, s[82:83]
	v_addc_co_u32_e64 v165, s[96:97], 0, v165, s[84:85]
	v_addc_co_u32_e64 v165, s[96:97], 0, v165, s[86:87]
	s_waitcnt lgkmcnt(7)
	v_cmp_gt_u32_e64 s[80:81], v184, v138
	v_cmp_gt_u32_e64 s[82:83], v185, v138
	v_cmp_gt_u32_e64 s[84:85], v186, v138
	v_cmp_gt_u32_e64 s[86:87], v187, v138
	v_addc_co_u32_e64 v136, s[96:97], 0, v136, s[80:81]
	v_addc_co_u32_e64 v136, s[96:97], 0, v136, s[82:83]
	v_addc_co_u32_e64 v136, s[96:97], 0, v136, s[84:85]
	v_addc_co_u32_e64 v136, s[96:97], 0, v136, s[86:87]
	v_cmp_gt_u32_e64 s[80:81], v188, v138
	v_cmp_gt_u32_e64 s[82:83], v189, v138
	v_cmp_gt_u32_e64 s[84:85], v190, v138
	v_cmp_gt_u32_e64 s[86:87], v191, v138
	v_addc_co_u32_e64 v165, s[96:97], 0, v165, s[80:81]
	v_addc_co_u32_e64 v165, s[96:97], 0, v165, s[82:83]
	v_addc_co_u32_e64 v165, s[96:97], 0, v165, s[84:85]
	v_addc_co_u32_e64 v165, s[96:97], 0, v165, s[86:87]
	s_waitcnt lgkmcnt(5)
	v_cmp_gt_u32_e64 s[80:81], v192, v138
	v_cmp_gt_u32_e64 s[82:83], v193, v138
	v_cmp_gt_u32_e64 s[84:85], v194, v138
	v_cmp_gt_u32_e64 s[86:87], v195, v138
	v_addc_co_u32_e64 v136, s[96:97], 0, v136, s[80:81]
	v_addc_co_u32_e64 v136, s[96:97], 0, v136, s[82:83]
	v_addc_co_u32_e64 v136, s[96:97], 0, v136, s[84:85]
	v_addc_co_u32_e64 v136, s[96:97], 0, v136, s[86:87]
	v_cmp_gt_u32_e64 s[80:81], v196, v138
	v_cmp_gt_u32_e64 s[82:83], v197, v138
	v_cmp_gt_u32_e64 s[84:85], v198, v138
	v_cmp_gt_u32_e64 s[86:87], v199, v138
	v_addc_co_u32_e64 v165, s[96:97], 0, v165, s[80:81]
	v_addc_co_u32_e64 v165, s[96:97], 0, v165, s[82:83]
	v_addc_co_u32_e64 v165, s[96:97], 0, v165, s[84:85]
	v_addc_co_u32_e64 v165, s[96:97], 0, v165, s[86:87]
	s_waitcnt lgkmcnt(3)
; #define LDS_WAIT() asm volatile("s_waitcnt lgkmcnt(0)" ::: "memory")
; __device__ __forceinline__ void peer_select_phase(const Args& a, int layer, LAS unsigned char* lds, int G, int bid) {
;     ...
; #pragma unroll 2
;         for (int m = 0; m < 50; m += 5) rank5(rc, (unsigned)__builtin_amdgcn_readlane((int)ck, m), (unsigned)__builtin_amdgcn_readlane((int)ck, m + 1), (unsigned)__builtin_amdgcn_readlane((int)ck, m + 2),
;                                               (unsigned)__builtin_amdgcn_readlane((int)ck, m + 3), (unsigned)__builtin_amdgcn_readlane((int)ck, m + 4), ck);
;         if (lane < 50 && rc < 16) { SV[32 + rc] = cv; SI[32 + rc] = ci * 16 + cj; }
;         LDS_WAIT();
;         {
;             const int ll = lane & 15;
;             const float ts = SV[32 + ll]; const int tp = SI[32 + ll];
;             const int e1 = SI[(tp >> 4) & 15], e2 = SI[16 + (tp & 15)];
;             const float mx = SV[32];
;             const float ex = __expf(rstd_t * (ts - mx));
;             float sm = ex; sm += __shfl_xor(sm, 8); sm += __shfl_xor(sm, 4); sm += __shfl_xor(sm, 2); sm += __shfl_xor(sm, 1);
;             if (lane < 16) { IDX[(size_t)tok * 128 + hd * 16 + lane] = e1 * 128 + e2; GATE[(size_t)tok * 128 + hd * 16 + lane] = ex / sm; }
	v_cmp_gt_u32_e64 s[80:81], v200, v138
	v_cmp_gt_u32_e64 s[82:83], v201, v138
	v_cmp_gt_u32_e64 s[84:85], v202, v138
	v_cmp_gt_u32_e64 s[86:87], v203, v138
	v_addc_co_u32_e64 v136, s[96:97], 0, v136, s[80:81]
	v_addc_co_u32_e64 v136, s[96:97], 0, v136, s[82:83]
	v_addc_co_u32_e64 v136, s[96:97], 0, v136, s[84:85]
	v_addc_co_u32_e64 v136, s[96:97], 0, v136, s[86:87]
	v_cmp_gt_u32_e64 s[80:81], v204, v138
	v_cmp_gt_u32_e64 s[82:83], v205, v138
	v_cmp_gt_u32_e64 s[84:85], v206, v138
	v_cmp_gt_u32_e64 s[86:87], v207, v138
	v_addc_co_u32_e64 v165, s[96:97], 0, v165, s[80:81]
	v_addc_co_u32_e64 v165, s[96:97], 0, v165, s[82:83]
	v_addc_co_u32_e64 v165, s[96:97], 0, v165, s[84:85]
	v_addc_co_u32_e64 v165, s[96:97], 0, v165, s[86:87]
	s_waitcnt lgkmcnt(1)
	v_cmp_gt_u32_e64 s[80:81], v208, v138
	v_cmp_gt_u32_e64 s[82:83], v209, v138
	v_cmp_gt_u32_e64 s[84:85], v210, v138
	v_cmp_gt_u32_e64 s[86:87], v211, v138
	v_addc_co_u32_e64 v136, s[96:97], 0, v136, s[80:81]
	v_addc_co_u32_e64 v136, s[96:97], 0, v136, s[82:83]
	v_addc_co_u32_e64 v136, s[96:97], 0, v136, s[84:85]
	v_addc_co_u32_e64 v136, s[96:97], 0, v136, s[86:87]
	v_cmp_gt_u32_e64 s[80:81], v212, v138
	v_cmp_gt_u32_e64 s[82:83], v213, v138
	v_cmp_gt_u32_e64 s[84:85], v214, v138
	v_cmp_gt_u32_e64 s[86:87], v215, v138
	v_addc_co_u32_e64 v165, s[96:97], 0, v165, s[80:81]
	v_addc_co_u32_e64 v165, s[96:97], 0, v165, s[82:83]
	v_addc_co_u32_e64 v165, s[96:97], 0, v165, s[84:85]
	v_addc_co_u32_e64 v165, s[96:97], 0, v165, s[86:87]
	s_waitcnt lgkmcnt(0)
	v_cmp_gt_u32_e64 s[80:81], v216, v138
	v_cmp_gt_u32_e64 s[82:83], v217, v138
	v_cmp_gt_u32_e64 s[84:85], v218, v138
	v_cmp_gt_u32_e64 s[86:87], v219, v138
	v_addc_co_u32_e64 v136, s[96:97], 0, v136, s[80:81]
	v_addc_co_u32_e64 v136, s[96:97], 0, v136, s[82:83]
	v_addc_co_u32_e64 v136, s[96:97], 0, v136, s[84:85]
	v_addc_co_u32_e64 v136, s[96:97], 0, v136, s[86:87]
	v_add_u32_e32 v136, v136, v165
	v_cmp_gt_i32_e32 vcc, 16, v136
	s_and_b64 s[12:13], s[6:7], vcc
	s_and_saveexec_b64 s[10:11], s[12:13]
	v_lshl_add_u32 v136, v136, 2, s50
	ds_write2_b32 v136, v131, v150 offset0:32 offset1:80
	s_or_b64 exec, exec, s[10:11]
	s_waitcnt lgkmcnt(0)
	v_mov_b32_e32 v131, s50
	ds_read_b32 v136, v151 offset:128
	ds_read_b32 v131, v131 offset:128
	v_and_b32_e32 v139, 64, v135
	v_xor_b32_e32 v138, 8, v135
	v_xor_b32_e32 v142, 2, v135
	v_xor_b32_e32 v143, 1, v135
	s_waitcnt lgkmcnt(0)
	v_sub_f32_e32 v131, v136, v131
	v_mul_f32_e32 v131, v156, v131
	v_mul_f32_e32 v131, 0x3fb8aa3b, v131
	v_exp_f32_e32 v141, v131
	v_add_u32_e32 v136, 64, v139
	v_cmp_lt_i32_e32 vcc, v138, v136
	v_xor_b32_e32 v139, 4, v135
	s_nop 0
	v_cndmask_b32_e32 v131, v135, v138, vcc
	v_lshlrev_b32_e32 v131, 2, v131
	ds_bpermute_b32 v138, v131, v141
	v_cmp_lt_i32_e32 vcc, v139, v136
	s_waitcnt lgkmcnt(0)
	v_add_f32_e32 v140, v141, v138
	v_cndmask_b32_e32 v139, v135, v139, vcc
	v_lshlrev_b32_e32 v138, 2, v139
	ds_bpermute_b32 v139, v138, v140
	v_cmp_lt_i32_e32 vcc, v142, v136
	s_waitcnt lgkmcnt(0)
	v_add_f32_e32 v140, v140, v139
	v_cndmask_b32_e32 v142, v135, v142, vcc
	v_lshlrev_b32_e32 v139, 2, v142
	ds_bpermute_b32 v142, v139, v140
	v_cmp_lt_i32_e32 vcc, v143, v136
	s_waitcnt lgkmcnt(0)
	v_add_f32_e32 v142, v140, v142
	v_cndmask_b32_e32 v143, v135, v143, vcc
	v_lshlrev_b32_e32 v140, 2, v143
	ds_bpermute_b32 v143, v140, v142
	s_and_saveexec_b64 s[10:11], s[8:9]
	s_cbranch_execz .LBB0_2181
	ds_read_b32 v144, v151 offset:320
	s_waitcnt lgkmcnt(1)
	v_add_f32_e32 v156, v142, v143
	s_ashr_i32 s12, s62, 3
	v_div_scale_f32 v158, s[34:35], v156, v156, v141
	s_waitcnt lgkmcnt(0)
	v_and_b32_e32 v145, 15, v144
	v_lshrrev_b32_e32 v144, 2, v144
	v_and_b32_e32 v144, 60, v144
	v_lshl_add_u32 v145, v145, 2, s50
	v_add_u32_e32 v144, s50, v144
	ds_read_b32 v145, v145 offset:256
	ds_read_b32 v144, v144 offset:192
	s_ashr_i32 s13, s12, 31
	v_rcp_f32_e32 v159, v158
	s_lshl_b64 s[12:13], s[12:13], 9
	v_lshl_or_b32 v142, v134, 2, s12
	v_mov_b32_e32 v143, s13
	s_waitcnt lgkmcnt(0)
	v_lshl_add_u32 v157, v144, 7, v145
	v_lshl_add_u64 v[144:145], s[20:21], 0, v[142:143]
	global_store_dword v[144:145], v157, off
	v_fma_f32 v144, -v158, v159, 1.0
	v_fmac_f32_e32 v159, v144, v159
	v_div_scale_f32 v144, vcc, v141, v156, v141
	v_mul_f32_e32 v145, v144, v159
	v_fma_f32 v157, -v158, v145, v144
	v_fmac_f32_e32 v145, v157, v159
	v_fma_f32 v144, -v158, v145, v144
	v_div_fmas_f32 v144, v144, v159, v145
	v_div_fixup_f32 v141, v144, v156, v141
	v_lshl_add_u64 v[142:143], s[22:23], 0, v[142:143]
	global_store_dword v[142:143], v141, off
